# phase-0 x->bf16 copy loop unrolled x4 (8 loads in flight per lane) on top of v15
# baseline (speedup 1.0000x reference)
.Lmy_x4_loop:
	v_readfirstlane_b32 s100, v6
	s_mul_i32 s101, s4, 3
	s_cmp_gt_i32 s100, s5
	s_cbranch_scc1 .LBB0_72
	s_add_i32 s100, s100, s101
	s_add_i32 s100, s100, 63
	s_cmp_gt_i32 s100, s5
	s_cbranch_scc1 .LBB0_71
	v_lshl_add_u64 v[18:19], v[2:3], 0, s[6:7]
	v_lshl_add_u64 v[20:21], v[18:19], 0, s[6:7]
	v_lshl_add_u64 v[22:23], v[20:21], 0, s[6:7]
	global_load_dwordx4 v[8:11], v[2:3], off
	global_load_dwordx4 v[12:15], v[2:3], off offset:16
	global_load_dwordx4 v[188:191], v[18:19], off
	global_load_dwordx4 v[192:195], v[18:19], off offset:16
	global_load_dwordx4 v[196:199], v[20:21], off
	global_load_dwordx4 v[200:203], v[20:21], off offset:16
	global_load_dwordx4 v[204:207], v[22:23], off
	global_load_dwordx4 v[208:211], v[22:23], off offset:16
	v_lshl_add_u64 v[2:3], v[22:23], 0, s[6:7]
	v_lshl_add_u64 v[16:17], s[78:79], 0, v[4:5]
	v_lshl_add_u64 v[24:25], v[16:17], 0, s[8:9]
	v_lshl_add_u64 v[26:27], v[24:25], 0, s[8:9]
	v_lshl_add_u64 v[28:29], v[26:27], 0, s[8:9]
	v_lshl_add_u64 v[4:5], v[4:5], 0, s[8:9]
	v_lshl_add_u64 v[4:5], v[4:5], 0, s[8:9]
	v_lshl_add_u64 v[4:5], v[4:5], 0, s[8:9]
	v_lshl_add_u64 v[4:5], v[4:5], 0, s[8:9]
	s_lshl_b32 s101, s4, 2
	v_add_u32_e32 v6, s101, v6
	s_waitcnt vmcnt(6)
	v_cvt_pk_bf16_f32 v8, v8, v9
	v_cvt_pk_bf16_f32 v9, v10, v11
	v_cvt_pk_bf16_f32 v10, v12, v13
	v_cvt_pk_bf16_f32 v11, v14, v15
	global_store_dwordx4 v[16:17], v[8:11], off
	s_waitcnt vmcnt(5)
	v_cvt_pk_bf16_f32 v188, v188, v189
	v_cvt_pk_bf16_f32 v189, v190, v191
	v_cvt_pk_bf16_f32 v190, v192, v193
	v_cvt_pk_bf16_f32 v191, v194, v195
	global_store_dwordx4 v[24:25], v[188:191], off
	s_waitcnt vmcnt(4)
	v_cvt_pk_bf16_f32 v196, v196, v197
	v_cvt_pk_bf16_f32 v197, v198, v199
	v_cvt_pk_bf16_f32 v198, v200, v201
	v_cvt_pk_bf16_f32 v199, v202, v203
	global_store_dwordx4 v[26:27], v[196:199], off
	s_waitcnt vmcnt(3)
	v_cvt_pk_bf16_f32 v204, v204, v205
	v_cvt_pk_bf16_f32 v205, v206, v207
	v_cvt_pk_bf16_f32 v206, v208, v209
	v_cvt_pk_bf16_f32 v207, v210, v211
	global_store_dwordx4 v[28:29], v[204:207], off
	s_branch .Lmy_x4_loop

	.amdhsa_kernel _Z6mk_fwd4Args
		.amdhsa_group_segment_fixed_size 0
		.amdhsa_private_segment_fixed_size 0
		.amdhsa_kernarg_size 464
		.amdhsa_user_sgpr_count 2
		.amdhsa_user_sgpr_dispatch_ptr 0
		.amdhsa_user_sgpr_queue_ptr 0
		.amdhsa_user_sgpr_kernarg_segment_ptr 1
		.amdhsa_user_sgpr_dispatch_id 0
		.amdhsa_user_sgpr_kernarg_preload_length 0
		.amdhsa_user_sgpr_kernarg_preload_offset 0
		.amdhsa_user_sgpr_private_segment_size 0
		.amdhsa_uses_dynamic_stack 0
		.amdhsa_enable_private_segment 0
		.amdhsa_system_sgpr_workgroup_id_x 1
		.amdhsa_system_sgpr_workgroup_id_y 0
		.amdhsa_system_sgpr_workgroup_id_z 0
		.amdhsa_system_sgpr_workgroup_info 0
		.amdhsa_system_vgpr_workitem_id 0
		.amdhsa_next_free_vgpr 240
		.amdhsa_next_free_sgpr 102
		.amdhsa_accum_offset 240
		.amdhsa_reserve_vcc 1
		.amdhsa_float_round_mode_32 0
		.amdhsa_float_round_mode_16_64 0
		.amdhsa_float_denorm_mode_32 3
		.amdhsa_float_denorm_mode_16_64 3
		.amdhsa_dx10_clamp 1
		.amdhsa_ieee_mode 1
		.amdhsa_fp16_overflow 0
		.amdhsa_tg_split 0
		.amdhsa_exception_fp_ieee_invalid_op 0
		.amdhsa_exception_fp_denorm_src 0
		.amdhsa_exception_fp_ieee_div_zero 0
		.amdhsa_exception_fp_ieee_overflow 0
		.amdhsa_exception_fp_ieee_underflow 0
		.amdhsa_exception_fp_ieee_inexact 0
		.amdhsa_exception_int_div_zero 0
	.end_amdhsa_kernel

amdhsa.kernels:
  - .agpr_count:     0
    .args:
      - .offset:         0
        .size:           208
        .value_kind:     by_value
      - .offset:         208
        .size:           4
        .value_kind:     hidden_block_count_x
      - .offset:         212
        .size:           4
        .value_kind:     hidden_block_count_y
      - .offset:         216
        .size:           4
        .value_kind:     hidden_block_count_z
      - .offset:         220
        .size:           2
        .value_kind:     hidden_group_size_x
      - .offset:         222
        .size:           2
        .value_kind:     hidden_group_size_y
      - .offset:         224
        .size:           2
        .value_kind:     hidden_group_size_z
      - .offset:         226
        .size:           2
        .value_kind:     hidden_remainder_x
      - .offset:         228
        .size:           2
        .value_kind:     hidden_remainder_y
      - .offset:         230
        .size:           2
        .value_kind:     hidden_remainder_z
      - .offset:         248
        .size:           8
        .value_kind:     hidden_global_offset_x
      - .offset:         256
        .size:           8
        .value_kind:     hidden_global_offset_y
      - .offset:         264
        .size:           8
        .value_kind:     hidden_global_offset_z
      - .offset:         272
        .size:           2
        .value_kind:     hidden_grid_dims
      - .offset:         328
        .size:           4
        .value_kind:     hidden_dynamic_lds_size
    .group_segment_fixed_size: 0
    .kernarg_segment_align: 8
    .kernarg_segment_size: 464
    .language:       OpenCL C
    .language_version:
      - 2
      - 0
    .max_flat_workgroup_size: 512
    .name:           _Z6mk_fwd4Args
    .private_segment_fixed_size: 0
    .sgpr_count:     108
    .sgpr_spill_count: 111
    .symbol:         _Z6mk_fwd4Args.kd
    .uniform_work_group_size: 1
    .uses_dynamic_stack: false
    .vgpr_count:     240
    .vgpr_spill_count: 0
    .wavefront_size: 64
